# dense attention: next unit's Q rows are loaded during the current unit's epilogue (flag in s32; skipped before a conversion slot and after the last unit)
# baseline (speedup 1.0000x reference)
.LBB0_238:
	s_add_u32 s10, s42, s0
	s_addc_u32 s11, s43, s1
	global_load_dwordx4 v[6:9], v5, s[10:11] offset:16
	global_load_dwordx4 v[10:13], v5, s[10:11]
	s_add_u32 s10, s44, s0
	s_addc_u32 s11, s45, s1
	global_load_dwordx4 v[14:17], v5, s[10:11]
	global_load_dwordx4 v[18:21], v5, s[10:11] offset:16
	s_add_u32 s0, s0, 32
	s_addc_u32 s1, s1, 0
	s_cmpk_eq_i32 s0, 0x100
	s_waitcnt vmcnt(2)
	v_max3_f32 v0, v2, |v10|, |v11|
	v_max3_f32 v0, v0, |v12|, |v13|
	s_waitcnt vmcnt(1)
	v_max3_f32 v2, v4, |v14|, |v15|
	v_max3_f32 v0, v0, |v6|, |v7|
	v_max3_f32 v4, v2, |v16|, |v17|
	v_max3_f32 v2, v0, |v8|, |v9|
	s_waitcnt vmcnt(0)
	v_max3_f32 v0, v4, |v18|, |v19|
	v_max3_f32 v4, v0, |v20|, |v21|
	s_cbranch_scc0 .LBB0_238
	v_mov_b32_e32 v0, 0x10000
	global_load_dword v5, v0, s[34:35] offset:256 sc1
	s_movk_i32 s10, 0x180
	s_and_b64 s[0:1], s[86:87], exec
	s_cselect_b32 s97, s10, 0xc00
	s_add_i32 s14, s95, s97
	s_cmpk_lt_i32 s94, 0x1800
	s_cselect_b64 s[60:61], -1, 0
	s_add_i32 s0, s94, 0xfffff000
	s_lshr_b32 s42, s0, 6
	s_mov_b32 s43, 0
	s_lshl_b64 s[0:1], s[42:43], 22
	s_lshl_b64 s[10:11], s[42:43], 24
	s_add_u32 s58, s24, s10
	s_addc_u32 s59, s25, s11
	s_lshr_b32 s10, s6, 25
	s_add_i32 s11, s94, s10
	s_ashr_i32 s10, s11, 7
	s_and_b32 s11, s11, 0xff80
	s_sub_i32 s44, s94, s11
	s_bfe_i32 s45, s44, 0x80000
	s_bfe_u32 s45, s45, 0x4000b
	s_add_i32 s45, s44, s45
	s_bfe_i32 s52, s45, 0x80000
	s_and_b32 s45, s45, 0xf0
	s_sub_i32 s44, s44, s45
	s_sext_i32_i8 s44, s44
	s_lshl_b32 s62, s44, 8
	s_mul_i32 s44, s9, s4
	s_ashr_i32 s11, s10, 31
	v_readlane_b32 s54, v254, 9
	s_sub_i32 s44, s7, s44
	s_lshl_b32 s15, s94, 5
	s_lshl_b32 s42, s94, 8
	s_lshl_b64 s[12:13], s[10:11], 25
	s_lshl_b64 s[10:11], s[10:11], 23
	s_lshl_b32 s55, s54, 1
	s_xor_b32 s8, s6, s8
	s_add_i32 s45, s9, 1
	s_sub_i32 s53, s44, s4
	s_cmp_ge_u32 s44, s4
	s_cselect_b32 s9, s45, s9
	s_cselect_b32 s44, s53, s44
	s_add_i32 s45, s9, 1
	s_cmp_ge_u32 s44, s4
	s_cselect_b32 s9, s45, s9
	s_xor_b32 s9, s9, s8
	s_sub_i32 s82, s9, s8
	s_add_i32 s8, s14, -1
	s_cmpk_lt_i32 s94, 0x1000
	s_cselect_b64 s[56:57], -1, 0
	s_add_u32 s45, s16, s0
	s_addc_u32 s53, s17, s1
	s_and_b32 s44, s15, 0x700
	s_and_b32 s64, s42, 0x700
	s_add_u32 s42, s20, s12
	s_addc_u32 s15, s21, s13
	v_mul_f32_e32 v0, 0x4f7ffffe, v3
	s_sext_i32_i16 s52, s52
	s_add_u32 s63, s40, s10
	v_cvt_u32_f32_e32 v0, v0
	s_addc_u32 s11, s41, s11
	s_lshl_b32 s0, s52, 4
	s_and_b32 s52, s0, 0xffffff00
	v_writelane_b32 v254, s55, 17
	s_or_b32 s0, s55, 1
	v_writelane_b32 v254, s0, 21
	s_mul_i32 s0, s82, s95
	s_sub_i32 s1, 1, s14
	s_sub_i32 s80, s94, s0
	s_xor_b32 s0, s8, s95
	s_max_i32 s1, s8, s1
	v_readfirstlane_b32 s8, v0
	s_mul_i32 s5, s5, s8
	s_mul_hi_u32 s5, s8, s5
	s_add_i32 s8, s8, s5
	s_mul_hi_u32 s5, s1, s8
	s_mul_i32 s8, s5, s4
	s_sub_i32 s1, s1, s8
	s_lshl_b32 s69, s54, 5
	s_ashr_i32 s0, s0, 31
	s_add_i32 s8, s5, 1
	s_sub_i32 s9, s1, s4
	s_cmp_ge_u32 s1, s4
	s_cselect_b32 s5, s8, s5
	s_cselect_b32 s1, s9, s1
	s_add_i32 s8, s5, 1
	s_cmp_ge_u32 s1, s4
	s_cselect_b32 s1, s8, s5
	s_xor_b32 s1, s1, s0
	s_sub_i32 s0, s1, s0
	s_abs_i32 s8, s0
	v_cvt_f32_u32_e32 v0, s8
	v_writelane_b32 v254, s60, 15
	s_mov_b64 s[86:87], -1
	s_cmp_ge_i32 s80, s97
	v_rcp_iflag_f32_e32 v0, v0
	v_writelane_b32 v254, s61, 16
	v_cndmask_b32_e64 v199, 0, 1, s[60:61]
	v_mul_f32_e32 v0, 0x4f7ffffe, v0
	v_cvt_u32_f32_e32 v0, v0
	s_nop 0
	v_readfirstlane_b32 s0, v0
	s_cbranch_scc1 .LBB0_355
	s_sub_i32 s1, 0, s8
	s_mul_i32 s1, s1, s0
	s_mul_hi_u32 s1, s0, s1
	s_add_i32 s0, s0, s1
	v_mul_f32_e32 v2, 0x4138aa3b, v2
	s_mul_hi_u32 s9, s7, s0
	v_mul_f32_e32 v2, v4, v2
	s_mov_b32 s0, 0x41600000
	s_waitcnt vmcnt(0)
	v_lshlrev_b32_e32 v4, 16, v5
	v_cmp_nge_f32_e32 vcc, s0, v2
	s_mov_b32 s0, 0x476a6000
	s_mul_i32 s9, s9, s8
	v_cmp_ngt_f32_e64 s[0:1], s0, v4
	s_sub_i32 s7, s7, s9
	s_or_b64 s[0:1], vcc, s[0:1]
	s_sub_i32 s9, s7, s8
	s_cmp_ge_u32 s7, s8
	s_cselect_b32 s7, s9, s7
	s_sub_i32 s9, s7, s8
	s_cmp_ge_u32 s7, s8
	s_cselect_b32 s7, s9, s7
	s_xor_b32 s7, s7, s6
	s_sub_i32 s81, s7, s6
	s_lshr_b32 s81, s94, 4
	s_add_i32 s7, s81, -12
	s_cmp_ge_u32 s81, 12
	s_cselect_b32 s81, s7, s81
	s_cmp_lg_u32 0, -1
	v_and_b32_e32 v0, 63, v235
	v_lshlrev_b32_e32 v2, 1, v235
	s_cselect_b32 s6, 0, 0
	v_cmp_gt_u32_e64 s[4:5], 32, v0
	v_mul_u32_u24_e32 v208, 0x300, v0
	v_lshlrev_b32_e32 v0, 3, v235
	v_and_b32_e32 v2, 32, v2
	s_add_i32 s7, s6, 0x12000
	v_and_b32_e32 v209, 24, v0
	v_and_b32_e32 v200, 56, v0
	v_add_u32_e32 v0, s7, v2
	s_add_u32 s7, s34, 0xc5600000
	v_writelane_b32 v254, s7, 20
	s_addc_u32 s7, s35, 0
	v_writelane_b32 v254, s7, 19
	v_writelane_b32 v254, s62, 22
	v_writelane_b32 v254, s64, 23
	s_add_u32 s12, s34, 0x5b600000
	v_writelane_b32 v254, s44, 24
	v_lshlrev_b32_e32 v4, 4, v235
	s_addc_u32 s13, s35, 0
	v_writelane_b32 v254, s52, 25
	v_bfe_u32 v6, v235, 5, 1
	v_and_b32_e32 v4, 0xc0, v4
	s_add_u32 s8, s34, 0x5ce00000
	v_writelane_b32 v254, s53, 26
	v_lshl_or_b32 v4, v6, 8, v4
	s_addc_u32 s9, s35, 0
	s_add_i32 s6, s6, 0xc000
	v_writelane_b32 v254, s11, 27
	s_movk_i32 s10, 0x800
	v_add3_u32 v214, v0, v209, v4
	v_add3_u32 v0, v2, s6, v209
	s_and_b64 s[6:7], s[56:57], exec
	v_writelane_b32 v254, s45, 28
	s_cselect_b32 s14, 0x1000, s10
	s_cselect_b32 s11, s11, s53
	v_writelane_b32 v254, s63, 29
	s_cselect_b32 s10, s63, s45
	v_writelane_b32 v254, s10, 30
	s_cselect_b32 s6, s52, s44
	s_cselect_b32 s54, s62, s64
	v_writelane_b32 v254, s11, 31
	v_writelane_b32 v254, s59, 32
	v_writelane_b32 v254, s15, 33
	v_writelane_b32 v254, s58, 34
	v_writelane_b32 v254, s42, 35
	s_cselect_b32 s15, s15, s59
	s_cselect_b32 s42, s42, s58
	v_writelane_b32 v254, s6, 36
	s_add_i32 s6, s6, s69
	s_ashr_i32 s7, s6, 31
	s_and_b64 s[10:11], s[56:57], exec
	s_cselect_b32 s10, 12, 11
	s_lshl_b64 s[6:7], s[6:7], s10
	s_lshl_b64 s[6:7], s[6:7], 2
	s_add_u32 s10, s42, s6
	s_mov_b32 s6, s54
	s_addc_u32 s11, s15, s7
	s_ashr_i32 s55, s54, 31
	v_writelane_b32 v254, s6, 37
	v_cndmask_b32_e64 v215, 0, 1, s[56:57]
	s_mov_b32 s45, s43
	v_writelane_b32 v254, s7, 38
	s_lshl_b64 s[6:7], s[54:55], 2
	s_add_u32 s6, s10, s6
	s_addc_u32 s7, s11, s7
	v_writelane_b32 v254, s6, 39
	s_mov_b32 s10, 0x7c000
	s_mov_b32 s11, 0x1e000
	v_writelane_b32 v254, s7, 40
	s_and_b64 s[6:7], s[56:57], exec
	s_cselect_b32 s6, s10, 0x3e000
	s_mov_b32 s7, s43
	v_writelane_b32 v254, s6, 41
	s_mov_b32 s10, 0x24000
	v_bfe_u32 v3, v235, 3, 3
	v_writelane_b32 v254, s7, 42
	s_mov_b32 s6, 0x78000
	s_cselect_b32 s6, s6, 0x3c000
	s_mov_b32 s7, s43
	v_writelane_b32 v254, s6, 43
	v_and_b32_e32 v207, 31, v235
	v_add_u32_e32 v8, 0, v2
	v_writelane_b32 v254, s7, 44
	s_mov_b32 s6, 0x74000
	s_cselect_b32 s6, s6, 0x3a000
	s_mov_b32 s7, s43
	v_writelane_b32 v254, s6, 45
	v_lshlrev_b32_e32 v203, 7, v3
	v_lshlrev_b32_e32 v5, 10, v6
	v_writelane_b32 v254, s7, 46
	s_mov_b32 s6, 0x70000
	s_cselect_b32 s6, s6, 0x38000
	s_mov_b32 s7, s43
	v_writelane_b32 v254, s6, 47
	v_lshlrev_b32_e32 v7, 4, v207
	v_mul_u32_u24_e32 v9, 0x600, v207
	v_writelane_b32 v254, s7, 48
	s_mov_b32 s6, 0x6c000
	s_cselect_b32 s6, s6, 0x36000
	s_mov_b32 s7, s43
	v_writelane_b32 v254, s6, 49
	v_add3_u32 v211, v8, v209, v4
	v_mul_u32_u24_e32 v196, 0x600, v3
	v_writelane_b32 v254, s7, 50
	s_mov_b32 s6, 0x68000
	s_cselect_b32 s6, s6, 0x34000
	s_mov_b32 s7, s43
	v_writelane_b32 v254, s6, 51
	v_bfe_u32 v201, v235, 2, 4
	v_lshlrev_b32_e32 v202, 9, v6
	v_writelane_b32 v254, s7, 52
	s_mov_b32 s6, 0x64000
	s_cselect_b32 s6, s6, 0x32000
	s_mov_b32 s7, s43
	v_writelane_b32 v254, s6, 53
	v_mov_b32_e32 v3, 0
	v_or_b32_e32 v204, 0x400, v203
	v_writelane_b32 v254, s7, 54
	s_mov_b32 s6, 0x60000
	s_cselect_b32 s6, s6, 0x30000
	s_mov_b32 s7, s43
	v_writelane_b32 v254, s6, 55
	v_or_b32_e32 v205, 0x800, v203
	v_or_b32_e32 v206, 0xc00, v203
	v_writelane_b32 v254, s7, 56
	s_mov_b32 s6, 0x5c000
	s_cselect_b32 s6, s6, 0x2e000
	s_mov_b32 s7, s43
	v_writelane_b32 v254, s6, 57
	v_lshl_or_b32 v198, v6, 3, v9
	v_add3_u32 v210, 0, v5, v7
	v_writelane_b32 v254, s7, 58
	s_mov_b32 s6, 0x58000
	s_cselect_b32 s6, s6, 0x2c000
	s_mov_b32 s7, s43
	v_writelane_b32 v254, s6, 59
	v_add_u32_e32 v212, 0xc000, v211
	v_lshlrev_b32_e32 v213, 4, v6
	v_writelane_b32 v254, s7, 60
	s_mov_b32 s6, 0x54000
	s_cselect_b32 s6, s6, 0x2a000
	s_mov_b32 s7, s43
	v_writelane_b32 v254, s6, 61
	s_mul_i32 s82, s82, s97
	s_mov_b32 s52, -4.0
	v_writelane_b32 v254, s7, 62
	s_mov_b32 s6, 0x50000
	s_cselect_b32 s6, s6, 0x28000
	s_mov_b32 s7, s43
	v_writelane_b32 v254, s6, 63
	s_mov_b32 s83, 0
	s_nop 0
	v_writelane_b32 v255, s7, 0
	s_mov_b32 s6, 0x4c000
	s_cselect_b32 s6, s6, 0x26000
	s_mov_b32 s7, s43
	v_writelane_b32 v255, s6, 1
	s_nop 1
	v_writelane_b32 v255, s7, 2
	s_mov_b32 s6, 0x48000
	s_cselect_b32 s6, s6, 0x24000
	s_mov_b32 s7, s43
	v_writelane_b32 v255, s6, 3
	s_nop 1
	v_writelane_b32 v255, s7, 4
	s_mov_b32 s6, 0x44000
	s_cselect_b32 s6, s6, 0x22000
	s_mov_b32 s7, s43
	v_writelane_b32 v255, s6, 5
	s_nop 1
	v_writelane_b32 v255, s7, 6
	s_lshl_b32 s6, s14, 6
	s_mov_b32 s7, s43
	v_writelane_b32 v255, s6, 7
	s_nop 1
	v_writelane_b32 v255, s7, 8
	v_writelane_b32 v255, s56, 9
	s_and_b64 s[6:7], s[56:57], exec
	s_cselect_b32 s6, 0x3c000, s11
	v_writelane_b32 v255, s57, 10
	s_mov_b32 s7, s43
	v_writelane_b32 v255, s6, 11
	s_cselect_b32 s10, s10, 0x12000
	s_mov_b32 s11, s43
	v_writelane_b32 v255, s7, 12
	s_mov_b32 s6, 0x1c000
	s_cselect_b32 s6, 0x38000, s6
	s_mov_b32 s7, s43
	v_writelane_b32 v255, s6, 13
	s_nop 1
	v_writelane_b32 v255, s7, 14
	s_mov_b32 s6, 0x1a000
	s_cselect_b32 s6, 0x34000, s6
	s_mov_b32 s7, s43
	v_writelane_b32 v255, s6, 15
	s_nop 1
	v_writelane_b32 v255, s7, 16
	s_mov_b32 s6, 0x18000
	s_cselect_b32 s44, 0x30000, s6
	v_writelane_b32 v255, s44, 17
	s_mov_b32 s7, 0x16000
	s_cselect_b32 s6, s6, 0xc000
	v_writelane_b32 v255, s45, 18
	s_cselect_b32 s44, 0x2c000, s7
	s_mov_b32 s45, s43
	v_writelane_b32 v255, s44, 19
	s_mov_b32 s7, 0x14000
	s_nop 0
	v_writelane_b32 v255, s45, 20
	s_cselect_b32 s44, 0x28000, s7
	s_mov_b32 s45, s43
	v_writelane_b32 v255, s44, 21
	s_mov_b32 s7, 0xe000
	s_nop 0
	v_writelane_b32 v255, s45, 22
	v_writelane_b32 v255, s10, 23
	s_mov_b32 s45, 0x41000000
	s_nop 0
	v_writelane_b32 v255, s11, 24
	s_cselect_b32 s10, 0x1c000, s7
	s_mov_b32 s11, s43
	v_writelane_b32 v255, s10, 25
	s_mov_b32 s7, s43
	s_nop 0
	v_writelane_b32 v255, s11, 26
	v_writelane_b32 v255, s6, 27
	s_mov_b32 s11, s43
	s_nop 0
	v_writelane_b32 v255, s7, 28
	s_mov_b32 s6, 0xa000
	s_cselect_b32 s6, 0x14000, s6
	s_mov_b32 s7, s43
	v_writelane_b32 v255, s6, 29
	s_nop 1
	v_writelane_b32 v255, s7, 30
	s_movk_i32 s6, 0x6000
	s_cselect_b32 s10, 0xc000, s6
	v_writelane_b32 v255, s10, 31
	v_add3_u32 v216, v0, v4, s6
	s_mov_b64 s[6:7], 0
	v_writelane_b32 v255, s11, 32
	s_lshl_b32 s10, s14, 5
	s_sub_u32 s10, 0, s10
	s_subb_u32 s11, 0, 0
	v_writelane_b32 v255, s10, 33
	s_nop 1
	v_writelane_b32 v255, s11, 34
	s_lshl_b32 s10, s14, 4
	s_sub_u32 s10, 0, s10
	s_subb_u32 s11, 0, 0
	v_writelane_b32 v255, s10, 35
	s_nop 1
	v_writelane_b32 v255, s11, 36
	s_lshl_b32 s10, s14, 3
	s_sub_u32 s10, 0, s10
	s_subb_u32 s11, 0, 0
	v_writelane_b32 v255, s10, 37
	s_nop 1
	v_writelane_b32 v255, s11, 38
	s_lshl_b32 s10, s14, 2
	s_sub_u32 s10, 0, s10
	s_subb_u32 s11, 0, 0
	v_writelane_b32 v255, s10, 39
	s_nop 1
	v_writelane_b32 v255, s11, 40
	s_mov_b32 s32, 0
	s_branch .LBB0_243
.LBB0_241:
	s_or_b64 exec, exec, s[14:15]
	s_mov_b32 s32, 0
	s_add_i32 s88, s80, s95
	s_cmp_ge_i32 s88, s97
	s_cbranch_scc1 .Lqpf_done
	s_add_i32 s89, s83, 1
	s_cmp_eq_u32 s89, s81
	s_cbranch_scc1 .Lqpf_done
	s_add_i32 s88, s88, s82
	s_and_b32 s54, s88, 63
	s_bfe_u32 s55, s88, 0x20006
	s_lshr_b32 s56, s88, 8
	s_cmp_ge_u32 s56, 6
	s_cselect_b32 s57, 1, 0
	s_cselect_b32 s58, 6, 0
	s_sub_i32 s56, s56, s58
	s_lshl_b32 s57, s57, 14
	s_lshl_b32 s54, s54, 8
	s_add_i32 s57, s57, s54
	s_lshl_b32 s54, s42, 5
	s_add_i32 s57, s57, s54
	s_mul_i32 s57, s57, 0xc00
	s_lshl_b32 s56, s56, 2
	s_add_i32 s56, s56, s55
	s_lshl_b32 s56, s56, 7
	s_add_i32 s57, s57, s56
	s_add_u32 s62, s73, s57
	s_addc_u32 s63, s75, 0
	v_lshlrev_b32_e32 v52, 1, v198
	global_load_dwordx4 v[140:143], v52, s[62:63]
	global_load_dwordx4 v[128:131], v52, s[62:63] offset:32
	global_load_dwordx4 v[136:139], v52, s[62:63] offset:64
	global_load_dwordx4 v[132:135], v52, s[62:63] offset:96
	s_mov_b32 s32, 1
.Lqpf_done:
	s_waitcnt lgkmcnt(0)
	v_add_u32_e32 v0, s11, v213
	ds_read_b128 v[36:39], v0 offset:128
	ds_read_b128 v[40:43], v0 offset:160
	s_add_u32 s10, s8, s90
	s_addc_u32 s11, s9, s91
	s_lshl_b32 s14, s42, 12
	s_waitcnt lgkmcnt(1)
	v_rcp_f32_e32 v2, v36
	v_rcp_f32_e32 v44, v37
	v_rcp_f32_e32 v45, v38
	v_rcp_f32_e32 v46, v39
	s_waitcnt lgkmcnt(0)
	v_rcp_f32_e32 v47, v40
	ds_read_b128 v[36:39], v0 offset:192
	v_rcp_f32_e32 v48, v41
	v_rcp_f32_e32 v49, v42
	v_rcp_f32_e32 v50, v43
	ds_read_b128 v[40:43], v0 offset:224
	s_waitcnt lgkmcnt(1)
	v_rcp_f32_e32 v0, v36
	v_rcp_f32_e32 v36, v37
	v_rcp_f32_e32 v37, v38
	v_rcp_f32_e32 v38, v39
	s_waitcnt lgkmcnt(0)
	v_rcp_f32_e32 v39, v40
	v_rcp_f32_e32 v40, v41
	v_rcp_f32_e32 v41, v42
	v_rcp_f32_e32 v42, v43
	s_add_i32 s14, s14, 0
	v_lshlrev_b32_e32 v43, 1, v207
	v_mul_f32_e32 v4, v4, v2
	v_mul_f32_e32 v2, v20, v2
	v_add3_u32 v43, s14, v202, v43
	v_cvt_pk_bf16_f32 v2, v2, s0
	ds_write_b16 v43, v2 offset:64
	v_mul_f32_e32 v2, v5, v44
	v_cvt_pk_bf16_f32 v2, v2, s0
	ds_write_b16 v43, v2 offset:128
	v_mul_f32_e32 v2, v21, v44
	v_cvt_pk_bf16_f32 v2, v2, s0
	ds_write_b16 v43, v2 offset:192
	v_mul_f32_e32 v2, v6, v45
	v_cvt_pk_bf16_f32 v2, v2, s0
	ds_write_b16 v43, v2 offset:256
	v_mul_f32_e32 v2, v22, v45
	v_cvt_pk_bf16_f32 v2, v2, s0
	ds_write_b16 v43, v2 offset:320
	v_mul_f32_e32 v2, v7, v46
	v_cvt_pk_bf16_f32 v2, v2, s0
	ds_write_b16 v43, v2 offset:384
	v_mul_f32_e32 v2, v23, v46
	v_cvt_pk_bf16_f32 v2, v2, s0
	ds_write_b16 v43, v2 offset:448
	v_mul_f32_e32 v2, v8, v47
	v_cvt_pk_bf16_f32 v2, v2, s0
	ds_write_b16 v43, v2 offset:1024
	v_mul_f32_e32 v2, v24, v47
	v_cvt_pk_bf16_f32 v2, v2, s0
	ds_write_b16 v43, v2 offset:1088
	v_mul_f32_e32 v2, v9, v48
	v_cvt_pk_bf16_f32 v2, v2, s0
	ds_write_b16 v43, v2 offset:1152
	v_mul_f32_e32 v2, v25, v48
	v_cvt_pk_bf16_f32 v2, v2, s0
	ds_write_b16 v43, v2 offset:1216
	v_mul_f32_e32 v2, v10, v49
	v_cvt_pk_bf16_f32 v2, v2, s0
	ds_write_b16 v43, v2 offset:1280
	v_mul_f32_e32 v2, v26, v49
	v_cvt_pk_bf16_f32 v2, v2, s0
	ds_write_b16 v43, v2 offset:1344
	v_mul_f32_e32 v2, v11, v50
	v_cvt_pk_bf16_f32 v2, v2, s0
	ds_write_b16 v43, v2 offset:1408
	v_mul_f32_e32 v2, v27, v50
	v_cvt_pk_bf16_f32 v2, v2, s0
	ds_write_b16 v43, v2 offset:1472
	v_mul_f32_e32 v2, v12, v0
	v_mul_f32_e32 v0, v28, v0
	v_cvt_pk_bf16_f32 v0, v0, s0
	ds_write_b16 v43, v0 offset:2112
	v_mul_f32_e32 v0, v13, v36
	v_cvt_pk_bf16_f32 v0, v0, s0
	ds_write_b16 v43, v0 offset:2176
	v_mul_f32_e32 v0, v29, v36
	v_cvt_pk_bf16_f32 v0, v0, s0
	ds_write_b16 v43, v0 offset:2240
	v_mul_f32_e32 v0, v14, v37
	v_cvt_pk_bf16_f32 v0, v0, s0
	ds_write_b16 v43, v0 offset:2304
	v_mul_f32_e32 v0, v30, v37
	v_cvt_pk_bf16_f32 v0, v0, s0
	ds_write_b16 v43, v0 offset:2368
	v_mul_f32_e32 v0, v15, v38
	v_cvt_pk_bf16_f32 v0, v0, s0
	ds_write_b16 v43, v0 offset:2432
	v_mul_f32_e32 v0, v31, v38
	v_cvt_pk_bf16_f32 v0, v0, s0
	ds_write_b16 v43, v0 offset:2496
	v_mul_f32_e32 v0, v16, v39
	v_cvt_pk_bf16_f32 v0, v0, s0
	ds_write_b16 v43, v0 offset:3072
	v_mul_f32_e32 v0, v32, v39
	v_cvt_pk_bf16_f32 v0, v0, s0
	ds_write_b16 v43, v0 offset:3136
	v_mul_f32_e32 v0, v17, v40
	v_cvt_pk_bf16_f32 v0, v0, s0
	ds_write_b16 v43, v0 offset:3200
	v_mul_f32_e32 v0, v33, v40
	v_cvt_pk_bf16_f32 v0, v0, s0
	ds_write_b16 v43, v0 offset:3264
	v_mul_f32_e32 v0, v18, v41
	v_cvt_pk_bf16_f32 v0, v0, s0
	ds_write_b16 v43, v0 offset:3328
	v_mul_f32_e32 v0, v34, v41
	v_cvt_pk_bf16_f32 v0, v0, s0
	ds_write_b16 v43, v0 offset:3392
	v_mul_f32_e32 v0, v19, v42
	v_cvt_pk_bf16_f32 v0, v0, s0
	v_cvt_pk_bf16_f32 v2, v2, s0
	ds_write_b16 v43, v0 offset:3456
	v_mul_f32_e32 v0, v35, v42
	v_cvt_pk_bf16_f32 v4, v4, s0
	ds_write_b16 v43, v2 offset:2048
	v_cvt_pk_bf16_f32 v0, v0, s0
	s_add_u32 s10, s10, vcc_lo
	v_lshlrev_b32_e32 v2, 1, v200
	ds_write_b16 v43, v4
	ds_write_b16 v43, v0 offset:3520
	s_addc_u32 s11, s11, vcc_hi
	v_add_u32_e32 v0, s14, v2
	s_waitcnt lgkmcnt(0)
	v_lshl_add_u64 v[8:9], s[10:11], 0, v[2:3]
	v_add_u32_e32 v2, v0, v203
	ds_read_b128 v[4:7], v2
	v_lshlrev_b32_e32 v2, 1, v196
	v_lshl_add_u64 v[12:13], v[8:9], 0, v[2:3]
	v_add_u32_e32 v2, v0, v204
	ds_read_b128 v[8:11], v2
	s_waitcnt lgkmcnt(1)
	global_store_dwordx4 v[12:13], v[4:7], off
	v_add_u32_e32 v2, v0, v205
	v_add_u32_e32 v0, v0, v206
	v_add_co_u32_e32 v4, vcc, 0x6000, v12
	s_nop 1
	v_addc_co_u32_e32 v5, vcc, 0, v13, vcc
	s_waitcnt lgkmcnt(0)
	global_store_dwordx4 v[4:5], v[8:11], off
	ds_read_b128 v[4:7], v2
	ds_read_b128 v[8:11], v0
	v_add_co_u32_e32 v14, vcc, 0xc000, v12
	s_nop 1
	v_addc_co_u32_e32 v15, vcc, 0, v13, vcc
	s_waitcnt lgkmcnt(1)
	global_store_dwordx4 v[14:15], v[4:7], off
	s_nop 1
	v_add_co_u32_e32 v4, vcc, 0x12000, v12
	s_nop 1
	v_addc_co_u32_e32 v5, vcc, 0, v13, vcc
	s_waitcnt lgkmcnt(0)
	global_store_dwordx4 v[4:5], v[8:11], off
	s_waitcnt lgkmcnt(0)
	s_barrier

.LBB0_334:
	s_and_b64 vcc, exec, s[60:61]
	s_cbranch_vccz .LBB0_242
	v_readlane_b32 s10, v254, 20
	s_add_u32 s10, s10, s56
	v_readlane_b32 s11, v254, 19
	s_addc_u32 s11, s11, s57
	s_add_u32 s14, s10, s58
	s_addc_u32 s15, s11, s59
	s_lshl_b64 s[90:91], s[54:55], 1
	s_add_u32 s10, s73, s90
	v_readfirstlane_b32 s11, v235
	s_addc_u32 s44, s75, s91
	s_lshr_b32 s42, s11, 6
	s_lshl_b32 s53, s42, 5
	s_mul_i32 s54, s42, 0xc000
	s_mul_hi_u32 s55, s53, 0x600
	s_lshl_b64 vcc, s[54:55], 1
	s_add_u32 s62, s10, vcc_lo
	s_addc_u32 s63, s44, vcc_hi
	s_lshl_b32 s10, s42, 4
	v_add_u32_e32 v165, s10, v208
	v_and_or_b32 v0, s10, 48, v201
	s_lshr_b32 s10, s11, 3
	s_and_b32 s10, s10, 0x1fffffe0
	s_lshl_b32 s44, s42, 10
	v_mov_b32_e32 v2, s10
	s_movk_i32 s10, 0x180
	s_cmp_lg_u32 0, -1
	v_mad_u32_u24 v0, v0, s10, v2
	s_cselect_b32 s10, 0, 0
	s_add_i32 s70, s44, s10
	v_or_b32_e32 v0, v0, v209
	s_add_i32 s10, s70, 0xc000
	s_mov_b32 m0, s70
	s_nop 0
	global_load_lds_dwordx4 v165, s[88:89]
	v_lshlrev_b32_e32 v164, 1, v0
	s_mov_b32 m0, s10
	s_nop 0
	global_load_lds_dwordx4 v164, s[14:15]
	s_add_u32 s54, s88, 0xc000
	s_addc_u32 s55, s89, 0
	s_add_i32 s71, s70, 0x2000
	s_mov_b32 m0, s71
	s_nop 0
	global_load_lds_dwordx4 v165, s[54:55]
	s_cmp_lg_u32 s32, 0
	s_cbranch_scc1 .Lqpf_skip
	global_load_dwordx4 v[140:143], v217, s[62:63]
	global_load_dwordx4 v[128:131], v217, s[62:63] offset:32
	global_load_dwordx4 v[136:139], v217, s[62:63] offset:64
	global_load_dwordx4 v[132:135], v217, s[62:63] offset:96
.Lqpf_skip:
	s_add_u32 s64, s88, 0x18000
	s_addc_u32 s65, s89, 0
	s_add_i32 s76, s70, 0x4000
	s_add_u32 s62, s88, 0x24000
	s_mov_b32 m0, s76
	s_nop 0
	global_load_lds_dwordx4 v165, s[64:65]
	s_addc_u32 s63, s89, 0
	s_add_i32 s77, s70, 0x6000
	s_mov_b32 m0, s77
	s_nop 0
	global_load_lds_dwordx4 v165, s[62:63]
	s_add_u32 s62, s14, 0xc000
	s_addc_u32 s63, s15, 0
	s_add_i32 s78, s70, 0xe000
	s_mov_b32 m0, s78
	s_nop 0
	global_load_lds_dwordx4 v164, s[62:63]
	s_add_u32 s62, s88, 0x30000
	s_addc_u32 s63, s89, 0
	s_add_i32 s79, s70, 0x8000
	s_mov_b32 m0, s79
	s_nop 0
	global_load_lds_dwordx4 v165, s[62:63]
	s_add_u32 s62, s88, 0x3c000
	s_addc_u32 s63, s89, 0
	s_add_i32 s85, s70, 0xa000
	s_mov_b32 m0, s85
	s_nop 0
	global_load_lds_dwordx4 v165, s[62:63]
	s_add_u32 s62, s14, 0x18000
	s_addc_u32 s63, s15, 0
	s_add_i32 s92, s70, 0x10000
	s_mov_b32 m0, s92
	s_nop 0
	global_load_lds_dwordx4 v164, s[62:63]
	s_add_u32 s62, s14, 0x24000
	s_addc_u32 s63, s15, 0
	s_add_i32 s93, s70, 0x12000
	s_mov_b32 m0, s93
	s_nop 0
	global_load_lds_dwordx4 v164, s[62:63]
	s_waitcnt vmcnt(7) lgkmcnt(0)
	s_barrier
	s_waitcnt vmcnt(22)
	ds_read_b128 v[36:39], v210
	s_waitcnt vmcnt(21)
	ds_read_b128 v[40:43], v210 offset:512
	s_mov_b32 s53, s52
	s_mov_b32 s54, s52
	s_mov_b32 s55, s52
	s_mov_b32 s56, s52
	s_mov_b32 s57, s52
	s_mov_b32 s58, s52
	s_mov_b32 s59, s52
	s_mov_b32 s60, s52
	s_mov_b32 s61, s52
	s_mov_b32 s62, s52
	s_mov_b32 s63, s52
	s_mov_b32 s64, s52
	s_mov_b32 s65, s52
	s_mov_b32 s66, s52
	s_mov_b32 s67, s52
	s_waitcnt vmcnt(13)
	v_mov_b64_e32 v[4:5], s[52:53]
	v_mov_b64_e32 v[6:7], s[54:55]
	v_mov_b64_e32 v[8:9], s[56:57]
	v_mov_b64_e32 v[10:11], s[58:59]
	v_mov_b64_e32 v[12:13], s[60:61]
	v_mov_b64_e32 v[14:15], s[62:63]
	v_mov_b64_e32 v[16:17], s[64:65]
	v_mov_b64_e32 v[18:19], s[66:67]
	v_mov_b32_e32 v148, 0
	v_mov_b32_e32 v2, 0
	v_mov_b32_e32 v72, 0
	s_mov_b32 s53, -5
	s_waitcnt lgkmcnt(1)
	v_mfma_f32_32x32x16_bf16 v[20:35], v[36:39], v[140:143], v[4:19]
	s_mov_b64 s[54:55], 0
	v_mov_b32_e32 v73, 0
	v_mov_b32_e32 v149, v148
	v_mov_b32_e32 v150, v148
	v_mov_b32_e32 v151, v148
	s_waitcnt lgkmcnt(0)
	v_mfma_f32_32x32x16_bf16 v[4:19], v[40:43], v[140:143], v[4:19]
	ds_read_b128 v[36:39], v210 offset:2048
	ds_read_b128 v[40:43], v210 offset:2560
	s_waitcnt lgkmcnt(1)
	v_mfma_f32_32x32x16_bf16 v[20:35], v[36:39], v[128:131], v[20:35]
	s_waitcnt lgkmcnt(0)
	v_mfma_f32_32x32x16_bf16 v[4:19], v[40:43], v[128:131], v[4:19]
	ds_read_b128 v[36:39], v210 offset:4096
	ds_read_b128 v[40:43], v210 offset:4608
	s_waitcnt lgkmcnt(1)
	v_mfma_f32_32x32x16_bf16 v[20:35], v[36:39], v[136:139], v[20:35]
	s_waitcnt lgkmcnt(0)
	v_mfma_f32_32x32x16_bf16 v[4:19], v[40:43], v[136:139], v[4:19]
	ds_read_b128 v[36:39], v210 offset:6144
	ds_read_b128 v[40:43], v210 offset:6656
	s_waitcnt lgkmcnt(1)
	v_mfma_f32_32x32x16_bf16 v[20:35], v[36:39], v[132:135], v[20:35]
	s_waitcnt lgkmcnt(0)
	v_mfma_f32_32x32x16_bf16 v[4:19], v[40:43], v[132:135], v[4:19]
	s_nop 15
	s_nop 7
	s_waitcnt vmcnt(4) lgkmcnt(0)
	s_barrier
	ds_read_b128 v[68:71], v210 offset:8192
	ds_read_b128 v[160:163], v210 offset:8704
	ds_read_b128 v[156:159], v210 offset:10240
	ds_read_b128 v[112:115], v210 offset:10752
	ds_read_b128 v[152:155], v210 offset:12288
	ds_read_b128 v[104:107], v210 offset:12800
	ds_read_b128 v[108:111], v210 offset:14336
	ds_read_b128 v[100:103], v210 offset:14848
	s_nop 1
	v_exp_f32_e32 v52, v20
	v_exp_f32_e32 v53, v21
	v_exp_f32_e32 v54, v22
	v_exp_f32_e32 v55, v23
	v_exp_f32_e32 v56, v24
	v_exp_f32_e32 v57, v25
	v_exp_f32_e32 v58, v26
	v_exp_f32_e32 v59, v27
	v_exp_f32_e32 v60, v28
	v_exp_f32_e32 v61, v29
	v_exp_f32_e32 v62, v30
	v_exp_f32_e32 v63, v31
	v_exp_f32_e32 v64, v32
	v_exp_f32_e32 v65, v33
	v_exp_f32_e32 v66, v34
	v_exp_f32_e32 v67, v35
	v_exp_f32_e32 v36, v4
	v_exp_f32_e32 v37, v5
	v_exp_f32_e32 v38, v6
	v_exp_f32_e32 v39, v7
	v_exp_f32_e32 v40, v8
	v_exp_f32_e32 v41, v9
	v_exp_f32_e32 v42, v10
	v_exp_f32_e32 v43, v11
	v_mov_b32_e32 v44, v12
	v_mov_b32_e32 v45, v13
	v_mov_b32_e32 v46, v14
	v_mov_b32_e32 v47, v15
	v_mov_b32_e32 v48, v16
	v_mov_b32_e32 v49, v17
	v_mov_b32_e32 v50, v18
	v_mov_b32_e32 v51, v19
	s_waitcnt vmcnt(4) lgkmcnt(0)
	s_barrier
	v_mov_b32_e32 v4, 0
	v_mov_b32_e32 v5, v2
	v_mov_b32_e32 v6, v2
	v_mov_b32_e32 v7, v2
	v_mov_b32_e32 v8, v2
	v_mov_b32_e32 v9, v2
	v_mov_b32_e32 v10, v2
	v_mov_b32_e32 v11, v2
	v_mov_b32_e32 v12, v2
	v_mov_b32_e32 v13, v2
	v_mov_b32_e32 v14, v2
	v_mov_b32_e32 v15, v2
	v_mov_b32_e32 v16, v2
	v_mov_b32_e32 v17, v2
	v_mov_b32_e32 v18, v2
	v_mov_b32_e32 v19, v2
	v_mov_b32_e32 v20, 0
	v_mov_b32_e32 v21, v2
	v_mov_b32_e32 v22, v2
	v_mov_b32_e32 v23, v2
	v_mov_b32_e32 v24, v2
	v_mov_b32_e32 v25, v2
	v_mov_b32_e32 v26, v2
	v_mov_b32_e32 v27, v2
	v_mov_b32_e32 v28, v2
	v_mov_b32_e32 v29, v2
	v_mov_b32_e32 v30, v2
	v_mov_b32_e32 v31, v2
	v_mov_b32_e32 v32, v2
	v_mov_b32_e32 v33, v2
	v_mov_b32_e32 v34, v2
	v_mov_b32_e32 v35, v2
